# v047 + ret_r1 second wave-max reduction via DPP instead of ds_bpermute butterfly
# baseline (speedup 1.0000x reference)
; template <int ISV>
; __device__ __forceinline__ void quant_finish(const QRow& q, unsigned char* qtab, float* scales, int e, int lane) {
;     float amax = 0.f;
; #pragma unroll
;     for (int j = 0; j < 8; ++j) amax = fmaxf(amax, fmaxf(fmaxf(fabsf(q.v[j].x), fabsf(q.v[j].y)), fmaxf(fabsf(q.v[j].z), fabsf(q.v[j].w))));
;     amax = wave_max(amax);
;     unsigned* qp = (unsigned*)qtab + (size_t)e * 64;
;     {
;         const float inv = amax > 0.f ? 127.0f / amax : 0.f;
;         if (lane == 0) scales[e] = amax * (1.0f / 127.0f);
; #pragma unroll
;         for (int j = 0; j < 8; ++j) {
;             qp[(size_t)j * 16384 * 64 + lane] = pack_i8x4(q.v[j], inv);
;         }
;     }
.LBB0_217:
	s_or_b64 exec, exec, s[6:7]
	v_div_scale_f32 v163, s[6:7], v162, v162, s13
	v_rcp_f32_e32 v164, v163
	v_div_scale_f32 v165, vcc, s13, v162, s13
	s_lshl_b64 s[6:7], s[48:49], 8
	v_fma_f32 v187, -v163, v164, 1.0
	v_fmac_f32_e32 v164, v187, v164
	v_mul_f32_e32 v187, v165, v164
	v_fma_f32 v189, -v163, v187, v165
	v_fmac_f32_e32 v187, v189, v164
	v_fma_f32 v163, -v163, v187, v165
	v_div_fmas_f32 v163, v163, v164, v187
	v_div_fixup_f32 v163, v163, v162, s13
	v_cmp_lt_f32_e32 vcc, 0, v162
	s_nop 1
	v_cndmask_b32_e32 v164, 0, v163, vcc
	v_fmaak_f32 v122, v122, v164, 0x4b400000
	v_fmaak_f32 v123, v123, v164, 0x4b400000
	v_fmaak_f32 v124, v124, v164, 0x4b400000
	v_fmaak_f32 v125, v125, v164, 0x4b400000
	v_lshl_add_u64 v[162:163], v[182:183], 0, s[6:7]
	v_perm_b32 v122, v123, v122, s14
	v_perm_b32 v123, v125, v124, s15
	v_or_b32_e32 v124, v122, v123
	v_add_co_u32_e32 v122, vcc, s16, v162
	v_fmaak_f32 v118, v118, v164, 0x4b400000
	v_fmaak_f32 v119, v119, v164, 0x4b400000
	v_fmaak_f32 v120, v120, v164, 0x4b400000
	v_fmaak_f32 v121, v121, v164, 0x4b400000
	v_addc_co_u32_e32 v123, vcc, 0, v163, vcc
	v_perm_b32 v118, v119, v118, s14
	v_perm_b32 v119, v121, v120, s15
	v_or_b32_e32 v120, v118, v119
	v_add_co_u32_e32 v118, vcc, s10, v162
	v_fmaak_f32 v114, v114, v164, 0x4b400000
	v_fmaak_f32 v115, v115, v164, 0x4b400000
	v_fmaak_f32 v116, v116, v164, 0x4b400000
	v_fmaak_f32 v117, v117, v164, 0x4b400000
	v_addc_co_u32_e32 v119, vcc, 0, v163, vcc
	v_perm_b32 v114, v115, v114, s14
	v_perm_b32 v115, v117, v116, s15
	v_or_b32_e32 v116, v114, v115
	v_add_co_u32_e32 v114, vcc, s17, v162
	v_fmaak_f32 v110, v110, v164, 0x4b400000
	v_fmaak_f32 v111, v111, v164, 0x4b400000
	v_fmaak_f32 v112, v112, v164, 0x4b400000
	v_fmaak_f32 v113, v113, v164, 0x4b400000
	v_addc_co_u32_e32 v115, vcc, 0, v163, vcc
	v_perm_b32 v110, v111, v110, s14
	v_perm_b32 v111, v113, v112, s15
	v_or_b32_e32 v112, v110, v111
	v_add_co_u32_e32 v110, vcc, s18, v162
	v_fmaak_f32 v106, v106, v164, 0x4b400000
	s_nop 0
	v_addc_co_u32_e32 v111, vcc, 0, v163, vcc
	v_fmaak_f32 v107, v107, v164, 0x4b400000
	v_fmaak_f32 v108, v108, v164, 0x4b400000
	v_fmaak_f32 v109, v109, v164, 0x4b400000
	global_store_dword v[110:111], v112, off
	v_perm_b32 v106, v107, v106, s14
	v_perm_b32 v107, v109, v108, s15
	s_waitcnt vmcnt(8)
	v_max_f32_e64 v109, |v97|, |v97|
	v_max_f32_e64 v110, |v96|, |v96|
	v_max_f32_e32 v109, v110, v109
	s_waitcnt vmcnt(7)
	v_max_f32_e64 v110, |v93|, |v93|
	v_max_f32_e64 v111, |v92|, |v92|
	v_max_f32_e32 v110, v111, v110
	v_max3_f32 v109, |v94|, |v95|, v109
	v_max3_f32 v110, |v90|, |v91|, v110
	v_max3_f32 v109, v109, 0, v110
	s_waitcnt vmcnt(6)
	v_max_f32_e64 v110, |v89|, |v89|
	v_max_f32_e64 v111, |v88|, |v88|
	v_max_f32_e32 v110, v111, v110
	s_waitcnt vmcnt(5)
	v_max_f32_e64 v111, |v85|, |v85|
	v_max_f32_e64 v112, |v84|, |v84|
	v_max_f32_e32 v111, v112, v111
	v_max3_f32 v110, |v86|, |v87|, v110
	v_max3_f32 v111, |v82|, |v83|, v111
	v_max3_f32 v109, v109, v110, v111
	s_waitcnt vmcnt(4)
	v_max_f32_e64 v110, |v81|, |v81|
	v_max_f32_e64 v111, |v80|, |v80|
	v_max_f32_e32 v110, v111, v110
	s_waitcnt vmcnt(3)
	v_max_f32_e64 v111, |v77|, |v77|
	v_max_f32_e64 v112, |v76|, |v76|
	v_max_f32_e32 v111, v112, v111
	v_max3_f32 v110, |v78|, |v79|, v110
	v_max3_f32 v111, |v74|, |v75|, v111
	v_max3_f32 v109, v109, v110, v111
	s_waitcnt vmcnt(2)
	v_max_f32_e64 v110, |v73|, |v73|
	v_max_f32_e64 v111, |v72|, |v72|
	v_max_f32_e32 v110, v111, v110
	s_waitcnt vmcnt(1)
	v_max_f32_e64 v111, |v69|, |v69|
	v_max_f32_e64 v112, |v68|, |v68|
	v_max_f32_e32 v111, v112, v111
	v_max3_f32 v110, |v70|, |v71|, v110
	v_max3_f32 v111, |v66|, |v67|, v111
	v_max3_f32 v109, v109, v110, v111
	s_nop 1
	v_or_b32_e32 v108, v106, v107
	v_add_co_u32_e32 v106, vcc, s19, v162
	v_fmaak_f32 v102, v102, v164, 0x4b400000
	s_nop 0
	v_addc_co_u32_e32 v107, vcc, 0, v163, vcc
	global_store_dword v[106:107], v108, off
	s_waitcnt lgkmcnt(0)
	s_nop 0
	v_max_f32_dpp v106, v109, v109 quad_perm:[1,0,3,2] row_mask:0xf bank_mask:0xf
	s_nop 1
	v_fmaak_f32 v103, v103, v164, 0x4b400000
	v_fmaak_f32 v104, v104, v164, 0x4b400000
	v_fmaak_f32 v105, v105, v164, 0x4b400000
	v_perm_b32 v102, v103, v102, s14
	v_perm_b32 v103, v105, v104, s15
	v_or_b32_e32 v104, v102, v103
	s_waitcnt lgkmcnt(0)
	s_nop 0
	v_max_f32_dpp v105, v106, v106 quad_perm:[2,3,0,1] row_mask:0xf bank_mask:0xf
	s_nop 1
	v_add_co_u32_e32 v102, vcc, s20, v162
	v_fmaak_f32 v98, v98, v164, 0x4b400000
	s_nop 0
	v_addc_co_u32_e32 v103, vcc, 0, v163, vcc
	s_waitcnt lgkmcnt(0)
	s_nop 0
	v_max_f32_dpp v105, v105, v105 row_half_mirror row_mask:0xf bank_mask:0xf
	s_nop 1
	global_store_dword v[102:103], v104, off
	v_fmaak_f32 v99, v99, v164, 0x4b400000
	v_fmaak_f32 v100, v100, v164, 0x4b400000
	v_fmaak_f32 v101, v101, v164, 0x4b400000
	s_waitcnt lgkmcnt(0)
	s_nop 0
	v_max_f32_dpp v102, v105, v105 row_mirror row_mask:0xf bank_mask:0xf
	s_nop 1
	v_perm_b32 v98, v99, v98, s14
	v_perm_b32 v99, v101, v100, s15
	v_or_b32_e32 v100, v98, v99
	v_fmaak_f32 v126, v126, v164, 0x4b400000
	s_waitcnt lgkmcnt(0)
	s_nop 0
	v_max_f32_dpp v101, v102, v102 row_bcast:15 row_mask:0xa bank_mask:0xf
	s_nop 1
	v_add_co_u32_e32 v98, vcc, s21, v162
	v_fmaak_f32 v127, v127, v164, 0x4b400000
	v_fmaak_f32 v128, v128, v164, 0x4b400000
	v_fmaak_f32 v129, v129, v164, 0x4b400000
	v_addc_co_u32_e32 v99, vcc, 0, v163, vcc
	v_perm_b32 v126, v127, v126, s14
	v_perm_b32 v127, v129, v128, s15
	global_store_dword v[98:99], v100, off
	s_waitcnt lgkmcnt(0)
	s_nop 0
	v_or_b32_e32 v126, v126, v127
	v_max_f32_dpp v98, v101, v101 row_bcast:31 row_mask:0xc bank_mask:0xf
	s_nop 1
	v_readlane_b32 s98, v98, 63
	s_nop 1
	v_mov_b32_e32 v98, s98
	global_store_dword v[162:163], v126, off
	global_store_dword v[122:123], v124, off
	global_store_dword v[118:119], v120, off
	global_store_dword v[114:115], v116, off
	s_and_saveexec_b64 s[6:7], s[38:39]
	s_cbranch_execz .LBB0_210
	s_lshl_b64 s[22:23], s[64:65], 2
	s_add_u32 s22, s50, s22
	s_addc_u32 s23, s51, s23
	v_mul_f32_e32 v99, 0x3c010204, v98
	global_store_dword v175, v99, s[22:23]
	s_branch .LBB0_210
